# plus: merged branch-output GEMM gate-rescale hook, its four drained load batches software-pipelined (second register set, counted waits)
# baseline (speedup 1.0000x reference)
.LBB0_473:
	ds_read_b128 v[138:141], v226
	ds_read_b128 v[142:145], v226 offset:1024
	ds_read_b128 v[146:149], v226 offset:2048
	ds_read_b128 v[150:153], v226 offset:3072
	ds_read_b128 v[154:157], v227
	ds_read_b128 v[158:161], v227 offset:1024
	ds_read_b128 v[162:165], v227 offset:2048
	ds_read_b128 v[166:169], v227 offset:3072
	v_lshl_add_u64 v[234:235], v[132:133], 0, s[66:67]
	s_add_i32 s92, s78, 0xc000
	v_lshl_add_u64 v[230:231], v[234:235], 0, s[22:23]
	s_mov_b32 m0, s92
	v_lshl_add_u64 v[236:237], v[130:131], 0, s[66:67]
	s_add_i32 s93, s78, 0xe000
	ds_read_b128 v[170:173], v228
	ds_read_b128 v[174:177], v228 offset:1024
	ds_read_b128 v[178:181], v228 offset:2048
	ds_read_b128 v[182:185], v228 offset:3072
	ds_read_b128 v[206:209], v228 offset:4096
	ds_read_b128 v[210:213], v228 offset:5120
	ds_read_b128 v[214:217], v228 offset:6144
	ds_read_b128 v[218:221], v228 offset:7168
	global_load_lds_dwordx4 v[230:231], off
	v_lshl_add_u64 v[230:231], v[236:237], 0, s[22:23]
	s_mov_b32 m0, s93
	s_nop 0
	global_load_lds_dwordx4 v[230:231], off
	s_waitcnt vmcnt(8)
	s_waitcnt lgkmcnt(0)
	s_barrier
	s_setprio 1
	s_waitcnt lgkmcnt(0)
	v_mfma_f32_16x16x32_bf16 v[30:33], v[138:141], v[170:173], v[30:33]
	v_mfma_f32_16x16x32_bf16 v[34:37], v[146:149], v[170:173], v[34:37]
	v_mfma_f32_16x16x32_bf16 v[50:53], v[138:141], v[178:181], v[50:53]
	v_mfma_f32_16x16x32_bf16 v[54:57], v[146:149], v[178:181], v[54:57]
	v_mfma_f32_16x16x32_bf16 v[74:77], v[138:141], v[206:209], v[74:77]
	v_mfma_f32_16x16x32_bf16 v[78:81], v[146:149], v[206:209], v[78:81]
	v_mfma_f32_16x16x32_bf16 v[98:101], v[138:141], v[214:217], v[98:101]
	v_mfma_f32_16x16x32_bf16 v[102:105], v[146:149], v[214:217], v[102:105]
	v_mfma_f32_16x16x32_bf16 v[30:33], v[142:145], v[174:177], v[30:33]
	v_mfma_f32_16x16x32_bf16 v[34:37], v[150:153], v[174:177], v[34:37]
	v_mfma_f32_16x16x32_bf16 v[50:53], v[142:145], v[182:185], v[50:53]
	v_mfma_f32_16x16x32_bf16 v[54:57], v[150:153], v[182:185], v[54:57]
	v_mfma_f32_16x16x32_bf16 v[74:77], v[142:145], v[210:213], v[74:77]
	v_mfma_f32_16x16x32_bf16 v[78:81], v[150:153], v[210:213], v[78:81]
	v_mfma_f32_16x16x32_bf16 v[98:101], v[142:145], v[218:221], v[98:101]
	v_mfma_f32_16x16x32_bf16 v[102:105], v[150:153], v[218:221], v[102:105]
	s_setprio 0
	s_setprio 1
	v_mfma_f32_16x16x32_bf16 v[42:45], v[154:157], v[170:173], v[42:45]
	v_mfma_f32_16x16x32_bf16 v[46:49], v[162:165], v[170:173], v[46:49]
	v_mfma_f32_16x16x32_bf16 v[62:65], v[154:157], v[178:181], v[62:65]
	v_mfma_f32_16x16x32_bf16 v[70:73], v[162:165], v[178:181], v[70:73]
	v_mfma_f32_16x16x32_bf16 v[86:89], v[154:157], v[206:209], v[86:89]
	v_mfma_f32_16x16x32_bf16 v[90:93], v[162:165], v[206:209], v[90:93]
	v_mfma_f32_16x16x32_bf16 v[110:113], v[154:157], v[214:217], v[110:113]
	v_mfma_f32_16x16x32_bf16 v[114:117], v[162:165], v[214:217], v[114:117]
	v_mfma_f32_16x16x32_bf16 v[42:45], v[158:161], v[174:177], v[42:45]
	v_mfma_f32_16x16x32_bf16 v[46:49], v[166:169], v[174:177], v[46:49]
	v_mfma_f32_16x16x32_bf16 v[62:65], v[158:161], v[182:185], v[62:65]
	v_mfma_f32_16x16x32_bf16 v[70:73], v[166:169], v[182:185], v[70:73]
	v_mfma_f32_16x16x32_bf16 v[86:89], v[158:161], v[210:213], v[86:89]
	v_mfma_f32_16x16x32_bf16 v[90:93], v[166:169], v[210:213], v[90:93]
	v_mfma_f32_16x16x32_bf16 v[110:113], v[158:161], v[218:221], v[110:113]
	v_mfma_f32_16x16x32_bf16 v[114:117], v[166:169], v[218:221], v[114:117]
	s_setprio 0
	s_barrier
	v_lshl_add_u64 v[238:239], v[136:137], 0, s[66:67]
	s_add_i32 s94, s86, s77
	v_lshl_add_u64 v[230:231], v[238:239], 0, s[40:41]
	s_mov_b32 m0, s94
	v_lshl_add_u64 v[240:241], v[134:135], 0, s[66:67]
	s_add_i32 s95, s94, 0x2000
	ds_read_b128 v[170:173], v228 offset:16384
	ds_read_b128 v[174:177], v228 offset:17408
	ds_read_b128 v[178:181], v228 offset:18432
	ds_read_b128 v[182:185], v228 offset:19456
	ds_read_b128 v[206:209], v228 offset:20480
	ds_read_b128 v[210:213], v228 offset:21504
	ds_read_b128 v[214:217], v228 offset:22528
	ds_read_b128 v[218:221], v228 offset:23552
	global_load_lds_dwordx4 v[230:231], off
	v_lshl_add_u64 v[230:231], v[240:241], 0, s[40:41]
	s_mov_b32 m0, s95
	s_add_i32 s96, s87, s77
	global_load_lds_dwordx4 v[230:231], off
	v_lshl_add_u64 v[230:231], v[238:239], 0, s[42:43]
	s_mov_b32 m0, s96
	s_add_i32 s97, s96, 0x2000
	global_load_lds_dwordx4 v[230:231], off
	v_lshl_add_u64 v[230:231], v[240:241], 0, s[42:43]
	s_mov_b32 m0, s97
	s_nop 0
	global_load_lds_dwordx4 v[230:231], off
	v_lshl_add_u64 v[230:231], v[234:235], 0, s[40:41]
	s_mov_b32 m0, s78
	s_nop 0
	global_load_lds_dwordx4 v[230:231], off
	v_lshl_add_u64 v[230:231], v[236:237], 0, s[40:41]
	s_mov_b32 m0, s79
	s_nop 0
	global_load_lds_dwordx4 v[230:231], off
	s_waitcnt vmcnt(8)
	s_waitcnt lgkmcnt(0)
	s_barrier
	s_setprio 1
	s_waitcnt lgkmcnt(0)
	v_mfma_f32_16x16x32_bf16 v[122:125], v[138:141], v[170:173], v[122:125]
	v_mfma_f32_16x16x32_bf16 v[126:129], v[146:149], v[170:173], v[126:129]
	v_mfma_f32_16x16x32_bf16 v[94:97], v[138:141], v[178:181], v[94:97]
	v_mfma_f32_16x16x32_bf16 v[82:85], v[146:149], v[178:181], v[82:85]
	v_mfma_f32_16x16x32_bf16 v[38:41], v[138:141], v[206:209], v[38:41]
	v_mfma_f32_16x16x32_bf16 v[26:29], v[146:149], v[206:209], v[26:29]
	v_mfma_f32_16x16x32_bf16 v[14:17], v[138:141], v[214:217], v[14:17]
	v_mfma_f32_16x16x32_bf16 v[10:13], v[146:149], v[214:217], v[10:13]
	v_mfma_f32_16x16x32_bf16 v[122:125], v[142:145], v[174:177], v[122:125]
	v_mfma_f32_16x16x32_bf16 v[126:129], v[150:153], v[174:177], v[126:129]
	v_mfma_f32_16x16x32_bf16 v[94:97], v[142:145], v[182:185], v[94:97]
	v_mfma_f32_16x16x32_bf16 v[82:85], v[150:153], v[182:185], v[82:85]
	v_mfma_f32_16x16x32_bf16 v[38:41], v[142:145], v[210:213], v[38:41]
	v_mfma_f32_16x16x32_bf16 v[26:29], v[150:153], v[210:213], v[26:29]
	v_mfma_f32_16x16x32_bf16 v[14:17], v[142:145], v[218:221], v[14:17]
	v_mfma_f32_16x16x32_bf16 v[10:13], v[150:153], v[218:221], v[10:13]
	s_setprio 0
	s_setprio 1
	v_mfma_f32_16x16x32_bf16 v[118:121], v[154:157], v[170:173], v[118:121]
	v_mfma_f32_16x16x32_bf16 v[106:109], v[162:165], v[170:173], v[106:109]
	v_mfma_f32_16x16x32_bf16 v[66:69], v[154:157], v[178:181], v[66:69]
	v_mfma_f32_16x16x32_bf16 v[58:61], v[162:165], v[178:181], v[58:61]
	v_mfma_f32_16x16x32_bf16 v[22:25], v[154:157], v[206:209], v[22:25]
	v_mfma_f32_16x16x32_bf16 v[18:21], v[162:165], v[206:209], v[18:21]
	v_mfma_f32_16x16x32_bf16 v[6:9], v[154:157], v[214:217], v[6:9]
	v_mfma_f32_16x16x32_bf16 v[2:5], v[162:165], v[214:217], v[2:5]
	v_mfma_f32_16x16x32_bf16 v[118:121], v[158:161], v[174:177], v[118:121]
	v_mfma_f32_16x16x32_bf16 v[106:109], v[166:169], v[174:177], v[106:109]
	v_mfma_f32_16x16x32_bf16 v[66:69], v[158:161], v[182:185], v[66:69]
	v_mfma_f32_16x16x32_bf16 v[58:61], v[166:169], v[182:185], v[58:61]
	v_mfma_f32_16x16x32_bf16 v[22:25], v[158:161], v[210:213], v[22:25]
	v_mfma_f32_16x16x32_bf16 v[18:21], v[166:169], v[210:213], v[18:21]
	v_mfma_f32_16x16x32_bf16 v[6:9], v[158:161], v[218:221], v[6:9]
	v_mfma_f32_16x16x32_bf16 v[2:5], v[166:169], v[218:221], v[2:5]
	s_setprio 0
	s_barrier
	s_add_i32 vcc_lo, 0, 0x18000
	s_add_i32 s60, 0, 0x1c000
	v_add_u32_e32 v155, vcc_lo, v224
	v_add_u32_e32 v156, s60, v224
	ds_read_b128 v[138:141], v155
	ds_read_b128 v[142:145], v155 offset:1024
	ds_read_b128 v[146:149], v155 offset:2048
	ds_read_b128 v[150:153], v155 offset:3072
	ds_read_b128 v[158:161], v156
	ds_read_b128 v[162:165], v156 offset:1024
	ds_read_b128 v[166:169], v156 offset:2048
	ds_read_b128 v[170:173], v156 offset:3072
	s_mov_b32 m0, s80
	v_lshl_add_u64 v[242:243], v[234:235], 0, s[42:43]
	ds_read_b128 v[174:177], v228 offset:32768
	ds_read_b128 v[178:181], v228 offset:33792
	ds_read_b128 v[182:185], v228 offset:34816
	ds_read_b128 v[206:209], v228 offset:35840
	ds_read_b128 v[210:213], v228 offset:36864
	ds_read_b128 v[214:217], v228 offset:37888
	ds_read_b128 v[218:221], v228 offset:38912
	ds_read_b128 v[230:233], v228 offset:39936
	global_load_lds_dwordx4 v[242:243], off
	v_lshl_add_u64 v[242:243], v[236:237], 0, s[42:43]
	s_mov_b32 m0, s81
	s_nop 0
	global_load_lds_dwordx4 v[242:243], off
	s_waitcnt vmcnt(8)
	s_waitcnt lgkmcnt(0)
	s_barrier
	s_setprio 1
	s_waitcnt lgkmcnt(0)
	v_mfma_f32_16x16x32_bf16 v[30:33], v[138:141], v[174:177], v[30:33]
	v_mfma_f32_16x16x32_bf16 v[34:37], v[146:149], v[174:177], v[34:37]
	v_mfma_f32_16x16x32_bf16 v[50:53], v[138:141], v[182:185], v[50:53]
	v_mfma_f32_16x16x32_bf16 v[54:57], v[146:149], v[182:185], v[54:57]
	v_mfma_f32_16x16x32_bf16 v[74:77], v[138:141], v[210:213], v[74:77]
	v_mfma_f32_16x16x32_bf16 v[78:81], v[146:149], v[210:213], v[78:81]
	v_mfma_f32_16x16x32_bf16 v[98:101], v[138:141], v[218:221], v[98:101]
	v_mfma_f32_16x16x32_bf16 v[102:105], v[146:149], v[218:221], v[102:105]
	v_mfma_f32_16x16x32_bf16 v[30:33], v[142:145], v[178:181], v[30:33]
	v_mfma_f32_16x16x32_bf16 v[34:37], v[150:153], v[178:181], v[34:37]
	v_mfma_f32_16x16x32_bf16 v[50:53], v[142:145], v[206:209], v[50:53]
	v_mfma_f32_16x16x32_bf16 v[54:57], v[150:153], v[206:209], v[54:57]
	v_mfma_f32_16x16x32_bf16 v[74:77], v[142:145], v[214:217], v[74:77]
	v_mfma_f32_16x16x32_bf16 v[78:81], v[150:153], v[214:217], v[78:81]
	v_mfma_f32_16x16x32_bf16 v[98:101], v[142:145], v[230:233], v[98:101]
	v_mfma_f32_16x16x32_bf16 v[102:105], v[150:153], v[230:233], v[102:105]
	s_setprio 0
	s_setprio 1
	v_mfma_f32_16x16x32_bf16 v[42:45], v[158:161], v[174:177], v[42:45]
	v_mfma_f32_16x16x32_bf16 v[46:49], v[166:169], v[174:177], v[46:49]
	v_mfma_f32_16x16x32_bf16 v[62:65], v[158:161], v[182:185], v[62:65]
	v_mfma_f32_16x16x32_bf16 v[70:73], v[166:169], v[182:185], v[70:73]
	v_mfma_f32_16x16x32_bf16 v[86:89], v[158:161], v[210:213], v[86:89]
	v_mfma_f32_16x16x32_bf16 v[90:93], v[166:169], v[210:213], v[90:93]
	v_mfma_f32_16x16x32_bf16 v[110:113], v[158:161], v[218:221], v[110:113]
	v_mfma_f32_16x16x32_bf16 v[114:117], v[166:169], v[218:221], v[114:117]
	v_mfma_f32_16x16x32_bf16 v[42:45], v[162:165], v[178:181], v[42:45]
	v_mfma_f32_16x16x32_bf16 v[46:49], v[170:173], v[178:181], v[46:49]
	v_mfma_f32_16x16x32_bf16 v[62:65], v[162:165], v[206:209], v[62:65]
	v_mfma_f32_16x16x32_bf16 v[70:73], v[170:173], v[206:209], v[70:73]
	v_mfma_f32_16x16x32_bf16 v[86:89], v[162:165], v[214:217], v[86:89]
	v_mfma_f32_16x16x32_bf16 v[90:93], v[170:173], v[214:217], v[90:93]
	v_mfma_f32_16x16x32_bf16 v[110:113], v[162:165], v[230:233], v[110:113]
	v_mfma_f32_16x16x32_bf16 v[114:117], v[170:173], v[230:233], v[114:117]
	s_setprio 0
	s_barrier
	s_add_i32 vcc_lo, vcc_lo, s77
	v_lshl_add_u64 v[242:243], v[238:239], 0, s[44:45]
	s_mov_b32 m0, vcc_lo
	s_add_i32 vcc_hi, vcc_lo, 0x2000
	ds_read_b128 v[174:177], v228 offset:49152
	ds_read_b128 v[178:181], v228 offset:50176
	ds_read_b128 v[182:185], v228 offset:51200
	ds_read_b128 v[206:209], v228 offset:52224
	ds_read_b128 v[210:213], v228 offset:53248
	ds_read_b128 v[214:217], v228 offset:54272
	ds_read_b128 v[218:221], v228 offset:55296
	ds_read_b128 v[230:233], v228 offset:56320
	global_load_lds_dwordx4 v[242:243], off
	v_lshl_add_u64 v[242:243], v[240:241], 0, s[44:45]
	s_mov_b32 m0, vcc_hi
	s_add_i32 s60, s60, s77
	global_load_lds_dwordx4 v[242:243], off
	v_lshl_add_u64 v[238:239], v[238:239], 0, s[46:47]
	s_mov_b32 m0, s60
	s_add_i32 s61, s60, 0x2000
	global_load_lds_dwordx4 v[238:239], off
	v_lshl_add_u64 v[238:239], v[240:241], 0, s[46:47]
	s_mov_b32 m0, s61
	v_lshl_add_u64 v[234:235], v[234:235], 0, s[44:45]
	global_load_lds_dwordx4 v[238:239], off
	s_mov_b32 m0, s83
	s_nop 0
	global_load_lds_dwordx4 v[234:235], off
	v_lshl_add_u64 v[234:235], v[236:237], 0, s[44:45]
	s_mov_b32 m0, s84
	s_nop 0
	global_load_lds_dwordx4 v[234:235], off
	s_waitcnt vmcnt(8)
	s_waitcnt lgkmcnt(0)
	s_barrier
	s_setprio 1
	s_waitcnt lgkmcnt(0)
	v_mfma_f32_16x16x32_bf16 v[122:125], v[138:141], v[174:177], v[122:125]
	v_mfma_f32_16x16x32_bf16 v[126:129], v[146:149], v[174:177], v[126:129]
	v_mfma_f32_16x16x32_bf16 v[94:97], v[138:141], v[182:185], v[94:97]
	v_mfma_f32_16x16x32_bf16 v[82:85], v[146:149], v[182:185], v[82:85]
	v_mfma_f32_16x16x32_bf16 v[38:41], v[138:141], v[210:213], v[38:41]
	v_mfma_f32_16x16x32_bf16 v[26:29], v[146:149], v[210:213], v[26:29]
	v_mfma_f32_16x16x32_bf16 v[14:17], v[138:141], v[218:221], v[14:17]
	v_mfma_f32_16x16x32_bf16 v[10:13], v[146:149], v[218:221], v[10:13]
	v_mfma_f32_16x16x32_bf16 v[122:125], v[142:145], v[178:181], v[122:125]
	v_mfma_f32_16x16x32_bf16 v[126:129], v[150:153], v[178:181], v[126:129]
	v_mfma_f32_16x16x32_bf16 v[94:97], v[142:145], v[206:209], v[94:97]
	v_mfma_f32_16x16x32_bf16 v[82:85], v[150:153], v[206:209], v[82:85]
	v_mfma_f32_16x16x32_bf16 v[38:41], v[142:145], v[214:217], v[38:41]
	v_mfma_f32_16x16x32_bf16 v[26:29], v[150:153], v[214:217], v[26:29]
	v_mfma_f32_16x16x32_bf16 v[14:17], v[142:145], v[230:233], v[14:17]
	v_mfma_f32_16x16x32_bf16 v[10:13], v[150:153], v[230:233], v[10:13]
	s_setprio 0
	s_setprio 1
	v_mfma_f32_16x16x32_bf16 v[118:121], v[158:161], v[174:177], v[118:121]
	v_mfma_f32_16x16x32_bf16 v[106:109], v[166:169], v[174:177], v[106:109]
	v_mfma_f32_16x16x32_bf16 v[66:69], v[158:161], v[182:185], v[66:69]
	v_mfma_f32_16x16x32_bf16 v[58:61], v[166:169], v[182:185], v[58:61]
	v_mfma_f32_16x16x32_bf16 v[22:25], v[158:161], v[210:213], v[22:25]
	v_mfma_f32_16x16x32_bf16 v[18:21], v[166:169], v[210:213], v[18:21]
	v_mfma_f32_16x16x32_bf16 v[6:9], v[158:161], v[218:221], v[6:9]
	v_mfma_f32_16x16x32_bf16 v[2:5], v[166:169], v[218:221], v[2:5]
	v_mfma_f32_16x16x32_bf16 v[118:121], v[162:165], v[178:181], v[118:121]
	v_mfma_f32_16x16x32_bf16 v[106:109], v[170:173], v[178:181], v[106:109]
	v_mfma_f32_16x16x32_bf16 v[66:69], v[162:165], v[206:209], v[66:69]
	v_mfma_f32_16x16x32_bf16 v[58:61], v[170:173], v[206:209], v[58:61]
	v_mfma_f32_16x16x32_bf16 v[22:25], v[162:165], v[214:217], v[22:25]
	v_mfma_f32_16x16x32_bf16 v[18:21], v[170:173], v[214:217], v[18:21]
	v_mfma_f32_16x16x32_bf16 v[6:9], v[162:165], v[230:233], v[6:9]
	v_mfma_f32_16x16x32_bf16 v[2:5], v[170:173], v[230:233], v[2:5]
	s_setprio 0
	s_barrier
	s_add_i32 s74, s74, 2
	s_add_u32 s66, s66, 0x100
	s_addc_u32 s67, s67, 0
	s_cmp_gt_u32 s74, 13
	s_cbranch_scc0 .LBB0_473
	v_add_u32_e32 v206, s90, v1
	s_movk_i32 s66, 0x3400
	v_mul_lo_u32 v130, v206, s66
	v_lshl_or_b32 v154, s35, 8, v225
	v_add_lshl_u32 v157, v130, v154, 1
	v_add_u32_e32 v130, 0x4800, v157
	global_load_dwordx4 v[158:161], v130, s[12:13]
	v_add_u32_e32 v130, 0x5800, v157
	global_load_dwordx4 v[162:165], v130, s[12:13]
	v_add_u32_e32 v130, 0x4900, v157
	global_load_dwordx4 v[146:149], v130, s[12:13]
	v_add_u32_e32 v130, 0x5900, v157
	global_load_dwordx4 v[150:153], v130, s[12:13]
	v_add_u32_e32 v130, 0x6c800, v157
	global_load_dwordx4 v[138:141], v130, s[12:13]
	v_add_u32_e32 v130, 0x6d800, v157
	global_load_dwordx4 v[142:145], v130, s[12:13]
	v_add_u32_e32 v134, 0x6c900, v157
	global_load_dwordx4 v[130:133], v134, s[12:13]
	v_add_u32_e32 v166, 0x6d900, v157
	global_load_dwordx4 v[134:137], v166, s[12:13]
	v_add_u32_e32 v220, 0xd4800, v157
	global_load_dwordx4 v[174:177], v220, s[12:13]
	v_add_u32_e32 v220, 0xd5800, v157
	global_load_dwordx4 v[178:181], v220, s[12:13]
	v_add_u32_e32 v220, 0xd4900, v157
	global_load_dwordx4 v[182:185], v220, s[12:13]
	v_add_u32_e32 v220, 0xd5900, v157
	global_load_dwordx4 v[208:211], v220, s[12:13]
	v_add_u32_e32 v220, 0x13c800, v157
	global_load_dwordx4 v[212:215], v220, s[12:13]
	v_add_u32_e32 v220, 0x13d800, v157
	global_load_dwordx4 v[216:219], v220, s[12:13]
	v_add_u32_e32 v230, 0x13c900, v157
	global_load_dwordx4 v[220:223], v230, s[12:13]
	v_add_u32_e32 v166, 0x13d900, v157
	global_load_dwordx4 v[230:233], v166, s[12:13]
	s_nop 0
	s_waitcnt vmcnt(8)
	s_nop 0
	v_lshlrev_b32_e32 v166, 16, v158
	v_and_b32_e32 v158, 0xffff0000, v158
	v_mul_f32_e32 v158, 0xbfb8aa3b, v158
	v_exp_f32_e32 v158, v158
	v_mul_f32_e32 v166, 0xbfb8aa3b, v166
	v_exp_f32_e32 v167, v166
	v_lshlrev_b32_e32 v166, 16, v162
	v_add_f32_e32 v158, 1.0, v158
	v_rcp_f32_e32 v169, v158
	v_lshlrev_b32_e32 v158, 16, v160
	v_mul_f32_e32 v158, 0xbfb8aa3b, v158
	v_exp_f32_e32 v158, v158
	v_and_b32_e32 v162, 0xffff0000, v162
	v_add_f32_e32 v167, 1.0, v167
	v_mul_f32_e32 v162, 0xbfb8aa3b, v162
	v_add_f32_e32 v158, 1.0, v158
	v_rcp_f32_e32 v172, v158
	v_and_b32_e32 v158, 0xffff0000, v160
	v_mul_f32_e32 v158, 0xbfb8aa3b, v158
	v_exp_f32_e32 v158, v158
	v_and_b32_e32 v160, 0xffff0000, v164
	v_rcp_f32_e32 v168, v167
	v_exp_f32_e32 v167, v162
	v_add_f32_e32 v158, 1.0, v158
	v_rcp_f32_e32 v173, v158
	v_lshlrev_b32_e32 v158, 16, v159
	v_lshlrev_b32_e32 v162, 16, v164
	v_mul_f32_e32 v160, 0xbfb8aa3b, v160
	v_mul_f32_e32 v158, 0xbfb8aa3b, v158
	v_and_b32_e32 v159, 0xffff0000, v159
	v_mul_f32_e32 v162, 0xbfb8aa3b, v162
	v_exp_f32_e32 v171, v160
	v_exp_f32_e32 v160, v158
	v_mul_f32_e32 v159, 0xbfb8aa3b, v159
	v_exp_f32_e32 v170, v162
	v_lshlrev_b32_e32 v158, 16, v163
	v_and_b32_e32 v162, 0xffff0000, v163
	v_exp_f32_e32 v163, v159
	v_mul_f32_e32 v158, 0xbfb8aa3b, v158
	v_add_f32_e32 v160, 1.0, v160
	v_mul_f32_e32 v159, 0xbfb8aa3b, v162
	v_exp_f32_e32 v158, v158
	v_exp_f32_e32 v159, v159
	v_rcp_f32_e32 v162, v160
	v_add_f32_e32 v160, 1.0, v163
	v_rcp_f32_e32 v163, v160
	v_pk_add_f32 v[158:159], v[158:159], 1.0 op_sel_hi:[1,0]
	v_mul_f32_e32 v166, 0xbfb8aa3b, v166
	v_exp_f32_e32 v166, v166
	v_pk_mul_f32 v[158:159], v[158:159], v[162:163]
	v_pk_add_f32 v[162:163], v[170:171], 1.0 op_sel_hi:[1,0]
	v_pk_mul_f32 v[32:33], v[32:33], v[158:159]
	v_lshlrev_b32_e32 v158, 16, v161
	v_mul_f32_e32 v158, 0xbfb8aa3b, v158
	v_exp_f32_e32 v159, v158
	v_and_b32_e32 v161, 0xffff0000, v161
	v_mul_f32_e32 v161, 0xbfb8aa3b, v161
	v_exp_f32_e32 v161, v161
	v_lshlrev_b32_e32 v158, 16, v165
	v_add_f32_e32 v160, 1.0, v159
	v_and_b32_e32 v159, 0xffff0000, v165
	v_mul_f32_e32 v158, 0xbfb8aa3b, v158
	v_mul_f32_e32 v159, 0xbfb8aa3b, v159
	v_exp_f32_e32 v158, v158
	v_exp_f32_e32 v159, v159
	v_add_f32_e32 v161, 1.0, v161
	v_rcp_f32_e32 v160, v160
	v_rcp_f32_e32 v161, v161
	v_pk_add_f32 v[158:159], v[158:159], 1.0 op_sel_hi:[1,0]
	v_pk_mul_f32 v[162:163], v[162:163], v[172:173]
	v_pk_add_f32 v[166:167], v[166:167], 1.0 op_sel_hi:[1,0]
	v_pk_mul_f32 v[158:159], v[158:159], v[160:161]
	v_pk_mul_f32 v[34:35], v[34:35], v[162:163]
	v_pk_mul_f32 v[36:37], v[36:37], v[158:159]
	v_lshlrev_b32_e32 v158, 16, v146
	v_and_b32_e32 v146, 0xffff0000, v146
	v_mul_f32_e32 v146, 0xbfb8aa3b, v146
	v_exp_f32_e32 v146, v146
	v_mul_f32_e32 v158, 0xbfb8aa3b, v158
	v_exp_f32_e32 v159, v158
	v_lshlrev_b32_e32 v158, 16, v150
	v_add_f32_e32 v146, 1.0, v146
	v_rcp_f32_e32 v161, v146
	v_lshlrev_b32_e32 v146, 16, v148
	v_mul_f32_e32 v146, 0xbfb8aa3b, v146
	v_exp_f32_e32 v146, v146
	v_and_b32_e32 v150, 0xffff0000, v150
	v_add_f32_e32 v159, 1.0, v159
	v_mul_f32_e32 v150, 0xbfb8aa3b, v150
	v_add_f32_e32 v146, 1.0, v146
	v_rcp_f32_e32 v164, v146
	v_and_b32_e32 v146, 0xffff0000, v148
	v_mul_f32_e32 v146, 0xbfb8aa3b, v146
	v_exp_f32_e32 v146, v146
	v_and_b32_e32 v148, 0xffff0000, v152
	v_rcp_f32_e32 v160, v159
	v_exp_f32_e32 v159, v150
	v_add_f32_e32 v146, 1.0, v146
	v_rcp_f32_e32 v165, v146
	v_lshlrev_b32_e32 v146, 16, v147
	v_lshlrev_b32_e32 v150, 16, v152
	v_mul_f32_e32 v148, 0xbfb8aa3b, v148
	v_mul_f32_e32 v146, 0xbfb8aa3b, v146
	v_and_b32_e32 v147, 0xffff0000, v147
	v_mul_f32_e32 v150, 0xbfb8aa3b, v150
	v_exp_f32_e32 v163, v148
	v_exp_f32_e32 v148, v146
	v_mul_f32_e32 v147, 0xbfb8aa3b, v147
	v_exp_f32_e32 v162, v150
	v_lshlrev_b32_e32 v146, 16, v151
	v_and_b32_e32 v150, 0xffff0000, v151
	v_exp_f32_e32 v151, v147
	v_mul_f32_e32 v146, 0xbfb8aa3b, v146
	v_add_f32_e32 v148, 1.0, v148
	v_mul_f32_e32 v147, 0xbfb8aa3b, v150
	v_exp_f32_e32 v146, v146
	v_exp_f32_e32 v147, v147
	v_rcp_f32_e32 v150, v148
	v_add_f32_e32 v148, 1.0, v151
	v_rcp_f32_e32 v151, v148
	v_pk_add_f32 v[146:147], v[146:147], 1.0 op_sel_hi:[1,0]
	v_mul_f32_e32 v158, 0xbfb8aa3b, v158
	v_exp_f32_e32 v158, v158
	v_pk_mul_f32 v[146:147], v[146:147], v[150:151]
	v_pk_add_f32 v[150:151], v[162:163], 1.0 op_sel_hi:[1,0]
	v_pk_mul_f32 v[44:45], v[44:45], v[146:147]
	v_lshlrev_b32_e32 v146, 16, v149
	v_mul_f32_e32 v146, 0xbfb8aa3b, v146
	v_exp_f32_e32 v147, v146
	v_and_b32_e32 v149, 0xffff0000, v149
	v_mul_f32_e32 v149, 0xbfb8aa3b, v149
	v_exp_f32_e32 v149, v149
	v_lshlrev_b32_e32 v146, 16, v153
	v_add_f32_e32 v148, 1.0, v147
	v_and_b32_e32 v147, 0xffff0000, v153
	v_mul_f32_e32 v146, 0xbfb8aa3b, v146
	v_mul_f32_e32 v147, 0xbfb8aa3b, v147
	v_exp_f32_e32 v146, v146
	v_exp_f32_e32 v147, v147
	v_add_f32_e32 v149, 1.0, v149
	v_rcp_f32_e32 v148, v148
	v_rcp_f32_e32 v149, v149
	v_pk_add_f32 v[146:147], v[146:147], 1.0 op_sel_hi:[1,0]
	v_pk_mul_f32 v[150:151], v[150:151], v[164:165]
	v_pk_mul_f32 v[166:167], v[166:167], v[168:169]
	v_pk_mul_f32 v[146:147], v[146:147], v[148:149]
	v_pk_mul_f32 v[46:47], v[46:47], v[150:151]
	v_pk_mul_f32 v[48:49], v[48:49], v[146:147]
	v_lshlrev_b32_e32 v146, 16, v138
	v_and_b32_e32 v138, 0xffff0000, v138
	v_mul_f32_e32 v138, 0xbfb8aa3b, v138
	v_exp_f32_e32 v138, v138
	v_mul_f32_e32 v146, 0xbfb8aa3b, v146
	v_exp_f32_e32 v147, v146
	v_lshlrev_b32_e32 v146, 16, v142
	v_add_f32_e32 v138, 1.0, v138
	v_rcp_f32_e32 v149, v138
	v_lshlrev_b32_e32 v138, 16, v140
	v_mul_f32_e32 v138, 0xbfb8aa3b, v138
	v_exp_f32_e32 v138, v138
	v_and_b32_e32 v142, 0xffff0000, v142
	v_add_f32_e32 v147, 1.0, v147
	v_mul_f32_e32 v142, 0xbfb8aa3b, v142
	v_add_f32_e32 v138, 1.0, v138
	v_rcp_f32_e32 v152, v138
	v_and_b32_e32 v138, 0xffff0000, v140
	v_mul_f32_e32 v138, 0xbfb8aa3b, v138
	v_exp_f32_e32 v138, v138
	v_and_b32_e32 v140, 0xffff0000, v144
	v_rcp_f32_e32 v148, v147
	v_exp_f32_e32 v147, v142
	v_add_f32_e32 v138, 1.0, v138
	v_rcp_f32_e32 v153, v138
	v_lshlrev_b32_e32 v138, 16, v139
	v_lshlrev_b32_e32 v142, 16, v144
	v_mul_f32_e32 v140, 0xbfb8aa3b, v140
	v_mul_f32_e32 v138, 0xbfb8aa3b, v138
	v_and_b32_e32 v139, 0xffff0000, v139
	v_mul_f32_e32 v142, 0xbfb8aa3b, v142
	v_exp_f32_e32 v151, v140
	v_exp_f32_e32 v140, v138
	v_mul_f32_e32 v139, 0xbfb8aa3b, v139
	v_exp_f32_e32 v150, v142
	v_lshlrev_b32_e32 v138, 16, v143
	v_and_b32_e32 v142, 0xffff0000, v143
	v_exp_f32_e32 v143, v139
	v_mul_f32_e32 v138, 0xbfb8aa3b, v138
	v_add_f32_e32 v140, 1.0, v140
	v_mul_f32_e32 v139, 0xbfb8aa3b, v142
	v_exp_f32_e32 v138, v138
	v_exp_f32_e32 v139, v139
	v_rcp_f32_e32 v142, v140
	v_add_f32_e32 v140, 1.0, v143
	v_rcp_f32_e32 v143, v140
	v_pk_add_f32 v[138:139], v[138:139], 1.0 op_sel_hi:[1,0]
	v_mul_f32_e32 v146, 0xbfb8aa3b, v146
	v_exp_f32_e32 v146, v146
	v_pk_mul_f32 v[138:139], v[138:139], v[142:143]
	v_pk_add_f32 v[142:143], v[150:151], 1.0 op_sel_hi:[1,0]
	v_pk_mul_f32 v[52:53], v[52:53], v[138:139]
	v_lshlrev_b32_e32 v138, 16, v141
	v_mul_f32_e32 v138, 0xbfb8aa3b, v138
	v_exp_f32_e32 v139, v138
	v_and_b32_e32 v141, 0xffff0000, v141
	v_mul_f32_e32 v141, 0xbfb8aa3b, v141
	v_exp_f32_e32 v141, v141
	v_lshlrev_b32_e32 v138, 16, v145
	v_add_f32_e32 v140, 1.0, v139
	v_and_b32_e32 v139, 0xffff0000, v145
	v_mul_f32_e32 v138, 0xbfb8aa3b, v138
	v_mul_f32_e32 v139, 0xbfb8aa3b, v139
	v_exp_f32_e32 v138, v138
	v_exp_f32_e32 v139, v139
	v_add_f32_e32 v141, 1.0, v141
	v_rcp_f32_e32 v140, v140
	v_rcp_f32_e32 v141, v141
	v_pk_add_f32 v[138:139], v[138:139], 1.0 op_sel_hi:[1,0]
	v_pk_mul_f32 v[142:143], v[142:143], v[152:153]
	v_pk_add_f32 v[158:159], v[158:159], 1.0 op_sel_hi:[1,0]
	v_pk_mul_f32 v[138:139], v[138:139], v[140:141]
	v_pk_mul_f32 v[54:55], v[54:55], v[142:143]
	v_pk_mul_f32 v[56:57], v[56:57], v[138:139]
	v_lshlrev_b32_e32 v138, 16, v130
	v_and_b32_e32 v130, 0xffff0000, v130
	v_mul_f32_e32 v130, 0xbfb8aa3b, v130
	v_exp_f32_e32 v130, v130
	v_mul_f32_e32 v138, 0xbfb8aa3b, v138
	v_exp_f32_e32 v139, v138
	v_lshlrev_b32_e32 v138, 16, v134
	v_add_f32_e32 v130, 1.0, v130
	v_rcp_f32_e32 v141, v130
	v_lshlrev_b32_e32 v130, 16, v132
	v_mul_f32_e32 v130, 0xbfb8aa3b, v130
	v_exp_f32_e32 v130, v130
	v_and_b32_e32 v134, 0xffff0000, v134
	v_add_f32_e32 v139, 1.0, v139
	v_mul_f32_e32 v134, 0xbfb8aa3b, v134
	v_add_f32_e32 v130, 1.0, v130
	v_rcp_f32_e32 v144, v130
	v_and_b32_e32 v130, 0xffff0000, v132
	v_mul_f32_e32 v130, 0xbfb8aa3b, v130
	v_exp_f32_e32 v130, v130
	v_and_b32_e32 v132, 0xffff0000, v136
	v_rcp_f32_e32 v140, v139
	v_exp_f32_e32 v139, v134
	v_add_f32_e32 v130, 1.0, v130
	v_rcp_f32_e32 v145, v130
	v_lshlrev_b32_e32 v130, 16, v131
	v_lshlrev_b32_e32 v134, 16, v136
	v_mul_f32_e32 v132, 0xbfb8aa3b, v132
	v_mul_f32_e32 v130, 0xbfb8aa3b, v130
	v_and_b32_e32 v131, 0xffff0000, v131
	v_mul_f32_e32 v134, 0xbfb8aa3b, v134
	v_exp_f32_e32 v143, v132
	v_exp_f32_e32 v132, v130
	v_mul_f32_e32 v131, 0xbfb8aa3b, v131
	v_exp_f32_e32 v142, v134
	v_lshlrev_b32_e32 v130, 16, v135
	v_and_b32_e32 v134, 0xffff0000, v135
	v_exp_f32_e32 v135, v131
	v_mul_f32_e32 v130, 0xbfb8aa3b, v130
	v_add_f32_e32 v132, 1.0, v132
	v_mul_f32_e32 v131, 0xbfb8aa3b, v134
	v_exp_f32_e32 v130, v130
	v_exp_f32_e32 v131, v131
	v_rcp_f32_e32 v134, v132
	v_add_f32_e32 v132, 1.0, v135
	v_rcp_f32_e32 v135, v132
	v_pk_add_f32 v[130:131], v[130:131], 1.0 op_sel_hi:[1,0]
	v_mul_f32_e32 v138, 0xbfb8aa3b, v138
	v_exp_f32_e32 v138, v138
	v_pk_mul_f32 v[130:131], v[130:131], v[134:135]
	v_pk_mul_f32 v[30:31], v[30:31], v[166:167]
	v_pk_mul_f32 v[64:65], v[64:65], v[130:131]
	v_lshlrev_b32_e32 v130, 16, v133
	v_mul_f32_e32 v130, 0xbfb8aa3b, v130
	v_exp_f32_e32 v131, v130
	v_and_b32_e32 v133, 0xffff0000, v133
	v_mul_f32_e32 v133, 0xbfb8aa3b, v133
	v_exp_f32_e32 v133, v133
	v_lshlrev_b32_e32 v130, 16, v137
	v_add_f32_e32 v132, 1.0, v131
	v_and_b32_e32 v131, 0xffff0000, v137
	v_mul_f32_e32 v130, 0xbfb8aa3b, v130
	v_mul_f32_e32 v131, 0xbfb8aa3b, v131
	v_exp_f32_e32 v130, v130
	v_exp_f32_e32 v131, v131
	v_add_f32_e32 v133, 1.0, v133
	v_rcp_f32_e32 v132, v132
	v_rcp_f32_e32 v133, v133
	v_pk_mul_f32 v[158:159], v[158:159], v[160:161]
	v_pk_add_f32 v[146:147], v[146:147], 1.0 op_sel_hi:[1,0]
	v_pk_mul_f32 v[42:43], v[42:43], v[158:159]
	v_pk_mul_f32 v[146:147], v[146:147], v[148:149]
	v_pk_add_f32 v[138:139], v[138:139], 1.0 op_sel_hi:[1,0]
	v_pk_add_f32 v[130:131], v[130:131], 1.0 op_sel_hi:[1,0]
	v_pk_add_f32 v[134:135], v[142:143], 1.0 op_sel_hi:[1,0]
	v_pk_mul_f32 v[50:51], v[50:51], v[146:147]
	v_pk_mul_f32 v[138:139], v[138:139], v[140:141]
	v_pk_mul_f32 v[134:135], v[134:135], v[144:145]
	v_pk_mul_f32 v[130:131], v[130:131], v[132:133]
	v_pk_mul_f32 v[62:63], v[62:63], v[138:139]
	v_pk_mul_f32 v[72:73], v[72:73], v[130:131]
	v_pk_mul_f32 v[70:71], v[70:71], v[134:135]
	s_nop 0
	v_add_u32_e32 v130, 0x344800, v157
	global_load_dwordx4 v[158:161], v130, s[12:13]
	v_add_u32_e32 v130, 0x345800, v157
	global_load_dwordx4 v[162:165], v130, s[12:13]
	v_add_u32_e32 v130, 0x344900, v157
	global_load_dwordx4 v[146:149], v130, s[12:13]
	v_add_u32_e32 v130, 0x345900, v157
	global_load_dwordx4 v[150:153], v130, s[12:13]
	v_add_u32_e32 v130, 0x3ac800, v157
	global_load_dwordx4 v[138:141], v130, s[12:13]
	v_add_u32_e32 v130, 0x3ad800, v157
	global_load_dwordx4 v[142:145], v130, s[12:13]
	v_add_u32_e32 v134, 0x3ac900, v157
	global_load_dwordx4 v[130:133], v134, s[12:13]
	v_add_u32_e32 v166, 0x3ad900, v157
	global_load_dwordx4 v[134:137], v166, s[12:13]
	s_nop 0
	s_waitcnt vmcnt(8)
	s_nop 0
	v_lshlrev_b32_e32 v166, 16, v174
	v_and_b32_e32 v174, 0xffff0000, v174
	v_mul_f32_e32 v174, 0xbfb8aa3b, v174
	v_exp_f32_e32 v174, v174
	v_mul_f32_e32 v166, 0xbfb8aa3b, v166
	v_exp_f32_e32 v167, v166
	v_lshlrev_b32_e32 v166, 16, v178
	v_add_f32_e32 v174, 1.0, v174
	v_rcp_f32_e32 v169, v174
	v_lshlrev_b32_e32 v174, 16, v176
	v_mul_f32_e32 v174, 0xbfb8aa3b, v174
	v_exp_f32_e32 v174, v174
	v_and_b32_e32 v178, 0xffff0000, v178
	v_add_f32_e32 v167, 1.0, v167
	v_mul_f32_e32 v178, 0xbfb8aa3b, v178
	v_add_f32_e32 v174, 1.0, v174
	v_rcp_f32_e32 v172, v174
	v_and_b32_e32 v174, 0xffff0000, v176
	v_mul_f32_e32 v174, 0xbfb8aa3b, v174
	v_exp_f32_e32 v174, v174
	v_and_b32_e32 v176, 0xffff0000, v180
	v_rcp_f32_e32 v168, v167
	v_exp_f32_e32 v167, v178
	v_add_f32_e32 v174, 1.0, v174
	v_rcp_f32_e32 v173, v174
	v_lshlrev_b32_e32 v174, 16, v175
	v_lshlrev_b32_e32 v178, 16, v180
	v_mul_f32_e32 v176, 0xbfb8aa3b, v176
	v_mul_f32_e32 v174, 0xbfb8aa3b, v174
	v_and_b32_e32 v175, 0xffff0000, v175
	v_mul_f32_e32 v178, 0xbfb8aa3b, v178
	v_exp_f32_e32 v171, v176
	v_exp_f32_e32 v176, v174
	v_mul_f32_e32 v175, 0xbfb8aa3b, v175
	v_exp_f32_e32 v170, v178
	v_lshlrev_b32_e32 v174, 16, v179
	v_and_b32_e32 v178, 0xffff0000, v179
	v_exp_f32_e32 v179, v175
	v_mul_f32_e32 v174, 0xbfb8aa3b, v174
	v_add_f32_e32 v176, 1.0, v176
	v_mul_f32_e32 v175, 0xbfb8aa3b, v178
	v_exp_f32_e32 v174, v174
	v_exp_f32_e32 v175, v175
	v_rcp_f32_e32 v178, v176
	v_add_f32_e32 v176, 1.0, v179
	v_rcp_f32_e32 v179, v176
	v_pk_add_f32 v[174:175], v[174:175], 1.0 op_sel_hi:[1,0]
	v_mul_f32_e32 v166, 0xbfb8aa3b, v166
	v_exp_f32_e32 v166, v166
	v_pk_mul_f32 v[174:175], v[174:175], v[178:179]
	v_pk_add_f32 v[178:179], v[170:171], 1.0 op_sel_hi:[1,0]
	v_pk_mul_f32 v[76:77], v[76:77], v[174:175]
	v_lshlrev_b32_e32 v174, 16, v177
	v_mul_f32_e32 v174, 0xbfb8aa3b, v174
	v_exp_f32_e32 v175, v174
	v_and_b32_e32 v177, 0xffff0000, v177
	v_mul_f32_e32 v177, 0xbfb8aa3b, v177
	v_exp_f32_e32 v177, v177
	v_lshlrev_b32_e32 v174, 16, v181
	v_add_f32_e32 v176, 1.0, v175
	v_and_b32_e32 v175, 0xffff0000, v181
	v_mul_f32_e32 v174, 0xbfb8aa3b, v174
	v_mul_f32_e32 v175, 0xbfb8aa3b, v175
	v_exp_f32_e32 v174, v174
	v_exp_f32_e32 v175, v175
	v_add_f32_e32 v177, 1.0, v177
	v_rcp_f32_e32 v176, v176
	v_rcp_f32_e32 v177, v177
	v_pk_add_f32 v[174:175], v[174:175], 1.0 op_sel_hi:[1,0]
	v_pk_mul_f32 v[178:179], v[178:179], v[172:173]
	v_pk_add_f32 v[166:167], v[166:167], 1.0 op_sel_hi:[1,0]
	v_pk_mul_f32 v[174:175], v[174:175], v[176:177]
	v_pk_mul_f32 v[78:79], v[78:79], v[178:179]
	v_pk_mul_f32 v[80:81], v[80:81], v[174:175]
	v_lshlrev_b32_e32 v174, 16, v182
	v_and_b32_e32 v182, 0xffff0000, v182
	v_mul_f32_e32 v182, 0xbfb8aa3b, v182
	v_exp_f32_e32 v182, v182
	v_mul_f32_e32 v174, 0xbfb8aa3b, v174
	v_exp_f32_e32 v175, v174
	v_lshlrev_b32_e32 v174, 16, v208
	v_add_f32_e32 v182, 1.0, v182
	v_rcp_f32_e32 v177, v182
	v_lshlrev_b32_e32 v182, 16, v184
	v_mul_f32_e32 v182, 0xbfb8aa3b, v182
	v_exp_f32_e32 v182, v182
	v_and_b32_e32 v208, 0xffff0000, v208
	v_add_f32_e32 v175, 1.0, v175
	v_mul_f32_e32 v208, 0xbfb8aa3b, v208
	v_add_f32_e32 v182, 1.0, v182
	v_rcp_f32_e32 v180, v182
	v_and_b32_e32 v182, 0xffff0000, v184
	v_mul_f32_e32 v182, 0xbfb8aa3b, v182
	v_exp_f32_e32 v182, v182
	v_and_b32_e32 v184, 0xffff0000, v210
	v_rcp_f32_e32 v176, v175
	v_exp_f32_e32 v175, v208
	v_add_f32_e32 v182, 1.0, v182
	v_rcp_f32_e32 v181, v182
	v_lshlrev_b32_e32 v182, 16, v183
	v_lshlrev_b32_e32 v208, 16, v210
	v_mul_f32_e32 v184, 0xbfb8aa3b, v184
	v_mul_f32_e32 v182, 0xbfb8aa3b, v182
	v_and_b32_e32 v183, 0xffff0000, v183
	v_mul_f32_e32 v208, 0xbfb8aa3b, v208
	v_exp_f32_e32 v179, v184
	v_exp_f32_e32 v184, v182
	v_mul_f32_e32 v183, 0xbfb8aa3b, v183
	v_exp_f32_e32 v178, v208
	v_lshlrev_b32_e32 v182, 16, v209
	v_and_b32_e32 v208, 0xffff0000, v209
	v_exp_f32_e32 v209, v183
	v_mul_f32_e32 v182, 0xbfb8aa3b, v182
	v_add_f32_e32 v184, 1.0, v184
	v_mul_f32_e32 v183, 0xbfb8aa3b, v208
	v_exp_f32_e32 v182, v182
	v_exp_f32_e32 v183, v183
	v_rcp_f32_e32 v208, v184
	v_add_f32_e32 v184, 1.0, v209
	v_rcp_f32_e32 v209, v184
	v_pk_add_f32 v[182:183], v[182:183], 1.0 op_sel_hi:[1,0]
	v_mul_f32_e32 v174, 0xbfb8aa3b, v174
	v_exp_f32_e32 v174, v174
	v_pk_mul_f32 v[182:183], v[182:183], v[208:209]
	v_pk_add_f32 v[208:209], v[178:179], 1.0 op_sel_hi:[1,0]
	v_pk_mul_f32 v[88:89], v[88:89], v[182:183]
	v_lshlrev_b32_e32 v182, 16, v185
	v_mul_f32_e32 v182, 0xbfb8aa3b, v182
	v_exp_f32_e32 v183, v182
	v_and_b32_e32 v185, 0xffff0000, v185
	v_mul_f32_e32 v185, 0xbfb8aa3b, v185
	v_exp_f32_e32 v185, v185
	v_lshlrev_b32_e32 v182, 16, v211
	v_add_f32_e32 v184, 1.0, v183
	v_and_b32_e32 v183, 0xffff0000, v211
	v_mul_f32_e32 v182, 0xbfb8aa3b, v182
	v_mul_f32_e32 v183, 0xbfb8aa3b, v183
	v_exp_f32_e32 v182, v182
	v_exp_f32_e32 v183, v183
	v_add_f32_e32 v185, 1.0, v185
	v_rcp_f32_e32 v184, v184
	v_rcp_f32_e32 v185, v185
	v_pk_add_f32 v[182:183], v[182:183], 1.0 op_sel_hi:[1,0]
	v_pk_mul_f32 v[208:209], v[208:209], v[180:181]
	v_pk_mul_f32 v[166:167], v[166:167], v[168:169]
	v_pk_mul_f32 v[182:183], v[182:183], v[184:185]
	v_pk_mul_f32 v[90:91], v[90:91], v[208:209]
	v_pk_mul_f32 v[92:93], v[92:93], v[182:183]
	v_lshlrev_b32_e32 v182, 16, v212
	v_and_b32_e32 v212, 0xffff0000, v212
	v_mul_f32_e32 v212, 0xbfb8aa3b, v212
	v_exp_f32_e32 v212, v212
	v_mul_f32_e32 v182, 0xbfb8aa3b, v182
	v_exp_f32_e32 v183, v182
	v_lshlrev_b32_e32 v182, 16, v216
	v_add_f32_e32 v212, 1.0, v212
	v_rcp_f32_e32 v185, v212
	v_lshlrev_b32_e32 v212, 16, v214
	v_mul_f32_e32 v212, 0xbfb8aa3b, v212
	v_exp_f32_e32 v212, v212
	v_and_b32_e32 v216, 0xffff0000, v216
	v_add_f32_e32 v183, 1.0, v183
	v_mul_f32_e32 v216, 0xbfb8aa3b, v216
	v_add_f32_e32 v212, 1.0, v212
	v_rcp_f32_e32 v210, v212
	v_and_b32_e32 v212, 0xffff0000, v214
	v_mul_f32_e32 v212, 0xbfb8aa3b, v212
	v_exp_f32_e32 v212, v212
	v_and_b32_e32 v214, 0xffff0000, v218
	v_rcp_f32_e32 v184, v183
	v_exp_f32_e32 v183, v216
	v_add_f32_e32 v212, 1.0, v212
	v_rcp_f32_e32 v211, v212
	v_lshlrev_b32_e32 v212, 16, v213
	v_lshlrev_b32_e32 v216, 16, v218
	v_mul_f32_e32 v214, 0xbfb8aa3b, v214
	v_mul_f32_e32 v212, 0xbfb8aa3b, v212
	v_and_b32_e32 v213, 0xffff0000, v213
	v_mul_f32_e32 v216, 0xbfb8aa3b, v216
	v_exp_f32_e32 v209, v214
	v_exp_f32_e32 v214, v212
	v_mul_f32_e32 v213, 0xbfb8aa3b, v213
	v_exp_f32_e32 v208, v216
	v_lshlrev_b32_e32 v212, 16, v217
	v_and_b32_e32 v216, 0xffff0000, v217
	v_exp_f32_e32 v217, v213
	v_mul_f32_e32 v212, 0xbfb8aa3b, v212
	v_add_f32_e32 v214, 1.0, v214
	v_mul_f32_e32 v213, 0xbfb8aa3b, v216
	v_exp_f32_e32 v212, v212
	v_exp_f32_e32 v213, v213
	v_rcp_f32_e32 v216, v214
	v_add_f32_e32 v214, 1.0, v217
	v_rcp_f32_e32 v217, v214
	v_pk_add_f32 v[212:213], v[212:213], 1.0 op_sel_hi:[1,0]
	v_mul_f32_e32 v182, 0xbfb8aa3b, v182
	v_exp_f32_e32 v182, v182
	v_pk_mul_f32 v[212:213], v[212:213], v[216:217]
	v_pk_add_f32 v[216:217], v[208:209], 1.0 op_sel_hi:[1,0]
	v_pk_mul_f32 v[100:101], v[100:101], v[212:213]
	v_lshlrev_b32_e32 v212, 16, v215
	v_mul_f32_e32 v212, 0xbfb8aa3b, v212
	v_exp_f32_e32 v213, v212
	v_and_b32_e32 v215, 0xffff0000, v215
	v_mul_f32_e32 v215, 0xbfb8aa3b, v215
	v_exp_f32_e32 v215, v215
	v_lshlrev_b32_e32 v212, 16, v219
	v_add_f32_e32 v214, 1.0, v213
	v_and_b32_e32 v213, 0xffff0000, v219
	v_mul_f32_e32 v212, 0xbfb8aa3b, v212
	v_mul_f32_e32 v213, 0xbfb8aa3b, v213
	v_exp_f32_e32 v212, v212
	v_exp_f32_e32 v213, v213
	v_add_f32_e32 v215, 1.0, v215
	v_rcp_f32_e32 v214, v214
	v_rcp_f32_e32 v215, v215
	v_pk_add_f32 v[212:213], v[212:213], 1.0 op_sel_hi:[1,0]
	v_pk_mul_f32 v[216:217], v[216:217], v[210:211]
	v_pk_add_f32 v[174:175], v[174:175], 1.0 op_sel_hi:[1,0]
	v_pk_mul_f32 v[212:213], v[212:213], v[214:215]
	v_pk_mul_f32 v[102:103], v[102:103], v[216:217]
	v_pk_mul_f32 v[104:105], v[104:105], v[212:213]
	v_lshlrev_b32_e32 v212, 16, v220
	v_and_b32_e32 v220, 0xffff0000, v220
	v_mul_f32_e32 v220, 0xbfb8aa3b, v220
	v_exp_f32_e32 v220, v220
	v_mul_f32_e32 v212, 0xbfb8aa3b, v212
	v_exp_f32_e32 v213, v212
	v_lshlrev_b32_e32 v212, 16, v230
	v_add_f32_e32 v220, 1.0, v220
	v_rcp_f32_e32 v215, v220
	v_lshlrev_b32_e32 v220, 16, v222
	v_mul_f32_e32 v220, 0xbfb8aa3b, v220
	v_exp_f32_e32 v220, v220
	v_and_b32_e32 v230, 0xffff0000, v230
	v_add_f32_e32 v213, 1.0, v213
	v_mul_f32_e32 v230, 0xbfb8aa3b, v230
	v_add_f32_e32 v220, 1.0, v220
	v_rcp_f32_e32 v218, v220
	v_and_b32_e32 v220, 0xffff0000, v222
	v_mul_f32_e32 v220, 0xbfb8aa3b, v220
	v_exp_f32_e32 v220, v220
	v_and_b32_e32 v222, 0xffff0000, v232
	v_rcp_f32_e32 v214, v213
	v_exp_f32_e32 v213, v230
	v_add_f32_e32 v220, 1.0, v220
	v_rcp_f32_e32 v219, v220
	v_lshlrev_b32_e32 v220, 16, v221
	v_lshlrev_b32_e32 v230, 16, v232
	v_mul_f32_e32 v222, 0xbfb8aa3b, v222
	v_mul_f32_e32 v220, 0xbfb8aa3b, v220
	v_and_b32_e32 v221, 0xffff0000, v221
	v_mul_f32_e32 v230, 0xbfb8aa3b, v230
	v_exp_f32_e32 v217, v222
	v_exp_f32_e32 v222, v220
	v_mul_f32_e32 v221, 0xbfb8aa3b, v221
	v_exp_f32_e32 v216, v230
	v_lshlrev_b32_e32 v220, 16, v231
	v_and_b32_e32 v230, 0xffff0000, v231
	v_exp_f32_e32 v231, v221
	v_mul_f32_e32 v220, 0xbfb8aa3b, v220
	v_add_f32_e32 v222, 1.0, v222
	v_mul_f32_e32 v221, 0xbfb8aa3b, v230
	v_exp_f32_e32 v220, v220
	v_exp_f32_e32 v221, v221
	v_rcp_f32_e32 v230, v222
	v_add_f32_e32 v222, 1.0, v231
	v_rcp_f32_e32 v231, v222
	v_pk_add_f32 v[220:221], v[220:221], 1.0 op_sel_hi:[1,0]
	v_mul_f32_e32 v212, 0xbfb8aa3b, v212
	v_exp_f32_e32 v212, v212
	v_pk_mul_f32 v[220:221], v[220:221], v[230:231]
	v_pk_mul_f32 v[74:75], v[74:75], v[166:167]
	v_pk_mul_f32 v[112:113], v[112:113], v[220:221]
	v_lshlrev_b32_e32 v220, 16, v223
	v_mul_f32_e32 v220, 0xbfb8aa3b, v220
	v_exp_f32_e32 v221, v220
	v_and_b32_e32 v223, 0xffff0000, v223
	v_mul_f32_e32 v223, 0xbfb8aa3b, v223
	v_exp_f32_e32 v223, v223
	v_lshlrev_b32_e32 v220, 16, v233
	v_add_f32_e32 v222, 1.0, v221
	v_and_b32_e32 v221, 0xffff0000, v233
	v_mul_f32_e32 v220, 0xbfb8aa3b, v220
	v_mul_f32_e32 v221, 0xbfb8aa3b, v221
	v_exp_f32_e32 v220, v220
	v_exp_f32_e32 v221, v221
	v_add_f32_e32 v223, 1.0, v223
	v_rcp_f32_e32 v222, v222
	v_rcp_f32_e32 v223, v223
	v_pk_mul_f32 v[174:175], v[174:175], v[176:177]
	v_pk_add_f32 v[182:183], v[182:183], 1.0 op_sel_hi:[1,0]
	v_pk_mul_f32 v[86:87], v[86:87], v[174:175]
	v_pk_mul_f32 v[182:183], v[182:183], v[184:185]
	v_pk_add_f32 v[212:213], v[212:213], 1.0 op_sel_hi:[1,0]
	v_pk_add_f32 v[220:221], v[220:221], 1.0 op_sel_hi:[1,0]
	v_pk_add_f32 v[230:231], v[216:217], 1.0 op_sel_hi:[1,0]
	v_pk_mul_f32 v[98:99], v[98:99], v[182:183]
	v_pk_mul_f32 v[212:213], v[212:213], v[214:215]
	v_pk_mul_f32 v[230:231], v[230:231], v[218:219]
	v_pk_mul_f32 v[220:221], v[220:221], v[222:223]
	v_pk_mul_f32 v[110:111], v[110:111], v[212:213]
	v_pk_mul_f32 v[116:117], v[116:117], v[220:221]
	v_pk_mul_f32 v[114:115], v[114:115], v[230:231]
	s_nop 0
	v_add_u32_e32 v220, 0x414800, v157
	global_load_dwordx4 v[174:177], v220, s[12:13]
	v_add_u32_e32 v220, 0x415800, v157
	global_load_dwordx4 v[178:181], v220, s[12:13]
	v_add_u32_e32 v220, 0x414900, v157
	global_load_dwordx4 v[182:185], v220, s[12:13]
	v_add_u32_e32 v220, 0x415900, v157
	global_load_dwordx4 v[208:211], v220, s[12:13]
	v_add_u32_e32 v220, 0x47c800, v157
	global_load_dwordx4 v[212:215], v220, s[12:13]
	v_add_u32_e32 v220, 0x47d800, v157
	global_load_dwordx4 v[216:219], v220, s[12:13]
	v_add_u32_e32 v230, 0x47c900, v157
	global_load_dwordx4 v[220:223], v230, s[12:13]
	v_add_u32_e32 v157, 0x47d900, v157
	global_load_dwordx4 v[230:233], v157, s[12:13]
	s_nop 0
	s_waitcnt vmcnt(8)
	s_nop 0
	v_lshlrev_b32_e32 v166, 16, v158
	v_and_b32_e32 v158, 0xffff0000, v158
	v_mul_f32_e32 v158, 0xbfb8aa3b, v158
	v_exp_f32_e32 v158, v158
	v_mul_f32_e32 v166, 0xbfb8aa3b, v166
	v_exp_f32_e32 v167, v166
	v_lshlrev_b32_e32 v166, 16, v162
	v_add_f32_e32 v158, 1.0, v158
	v_rcp_f32_e32 v169, v158
	v_lshlrev_b32_e32 v158, 16, v160
	v_mul_f32_e32 v158, 0xbfb8aa3b, v158
	v_exp_f32_e32 v158, v158
	v_and_b32_e32 v162, 0xffff0000, v162
	v_add_f32_e32 v167, 1.0, v167
	v_mul_f32_e32 v162, 0xbfb8aa3b, v162
	v_add_f32_e32 v158, 1.0, v158
	v_rcp_f32_e32 v172, v158
	v_and_b32_e32 v158, 0xffff0000, v160
	v_mul_f32_e32 v158, 0xbfb8aa3b, v158
	v_exp_f32_e32 v158, v158
	v_and_b32_e32 v160, 0xffff0000, v164
	v_rcp_f32_e32 v168, v167
	v_exp_f32_e32 v167, v162
	v_add_f32_e32 v158, 1.0, v158
	v_rcp_f32_e32 v173, v158
	v_lshlrev_b32_e32 v158, 16, v159
	v_lshlrev_b32_e32 v162, 16, v164
	v_mul_f32_e32 v160, 0xbfb8aa3b, v160
	v_mul_f32_e32 v158, 0xbfb8aa3b, v158
	v_and_b32_e32 v159, 0xffff0000, v159
	v_mul_f32_e32 v162, 0xbfb8aa3b, v162
	v_exp_f32_e32 v171, v160
	v_exp_f32_e32 v160, v158
	v_mul_f32_e32 v159, 0xbfb8aa3b, v159
	v_exp_f32_e32 v170, v162
	v_lshlrev_b32_e32 v158, 16, v163
	v_and_b32_e32 v162, 0xffff0000, v163
	v_exp_f32_e32 v163, v159
	v_mul_f32_e32 v158, 0xbfb8aa3b, v158
	v_add_f32_e32 v160, 1.0, v160
	v_mul_f32_e32 v159, 0xbfb8aa3b, v162
	v_exp_f32_e32 v158, v158
	v_exp_f32_e32 v159, v159
	v_rcp_f32_e32 v162, v160
	v_add_f32_e32 v160, 1.0, v163
	v_rcp_f32_e32 v163, v160
	v_pk_add_f32 v[158:159], v[158:159], 1.0 op_sel_hi:[1,0]
	v_mul_f32_e32 v166, 0xbfb8aa3b, v166
	v_exp_f32_e32 v166, v166
	v_pk_mul_f32 v[158:159], v[158:159], v[162:163]
	v_pk_add_f32 v[162:163], v[170:171], 1.0 op_sel_hi:[1,0]
	v_pk_mul_f32 v[124:125], v[124:125], v[158:159]
	v_lshlrev_b32_e32 v158, 16, v161
	v_mul_f32_e32 v158, 0xbfb8aa3b, v158
	v_exp_f32_e32 v159, v158
	v_and_b32_e32 v161, 0xffff0000, v161
	v_mul_f32_e32 v161, 0xbfb8aa3b, v161
	v_exp_f32_e32 v161, v161
	v_lshlrev_b32_e32 v158, 16, v165
	v_add_f32_e32 v160, 1.0, v159
	v_and_b32_e32 v159, 0xffff0000, v165
	v_mul_f32_e32 v158, 0xbfb8aa3b, v158
	v_mul_f32_e32 v159, 0xbfb8aa3b, v159
	v_exp_f32_e32 v158, v158
	v_exp_f32_e32 v159, v159
	v_add_f32_e32 v161, 1.0, v161
	v_rcp_f32_e32 v160, v160
	v_rcp_f32_e32 v161, v161
	v_pk_add_f32 v[158:159], v[158:159], 1.0 op_sel_hi:[1,0]
	v_pk_mul_f32 v[162:163], v[162:163], v[172:173]
	v_pk_add_f32 v[166:167], v[166:167], 1.0 op_sel_hi:[1,0]
	v_pk_mul_f32 v[158:159], v[158:159], v[160:161]
	v_pk_mul_f32 v[126:127], v[126:127], v[162:163]
	v_pk_mul_f32 v[128:129], v[128:129], v[158:159]
	v_lshlrev_b32_e32 v158, 16, v146
	v_and_b32_e32 v146, 0xffff0000, v146
	v_mul_f32_e32 v146, 0xbfb8aa3b, v146
	v_exp_f32_e32 v146, v146
	v_mul_f32_e32 v158, 0xbfb8aa3b, v158
	v_exp_f32_e32 v159, v158
	v_lshlrev_b32_e32 v158, 16, v150
	v_add_f32_e32 v146, 1.0, v146
	v_rcp_f32_e32 v161, v146
	v_lshlrev_b32_e32 v146, 16, v148
	v_mul_f32_e32 v146, 0xbfb8aa3b, v146
	v_exp_f32_e32 v146, v146
	v_and_b32_e32 v150, 0xffff0000, v150
	v_add_f32_e32 v159, 1.0, v159
	v_mul_f32_e32 v150, 0xbfb8aa3b, v150
	v_add_f32_e32 v146, 1.0, v146
	v_rcp_f32_e32 v164, v146
	v_and_b32_e32 v146, 0xffff0000, v148
	v_mul_f32_e32 v146, 0xbfb8aa3b, v146
	v_exp_f32_e32 v146, v146
	v_and_b32_e32 v148, 0xffff0000, v152
	v_rcp_f32_e32 v160, v159
	v_exp_f32_e32 v159, v150
	v_add_f32_e32 v146, 1.0, v146
	v_rcp_f32_e32 v165, v146
	v_lshlrev_b32_e32 v146, 16, v147
	v_lshlrev_b32_e32 v150, 16, v152
	v_mul_f32_e32 v148, 0xbfb8aa3b, v148
	v_mul_f32_e32 v146, 0xbfb8aa3b, v146
	v_and_b32_e32 v147, 0xffff0000, v147
	v_mul_f32_e32 v150, 0xbfb8aa3b, v150
	v_exp_f32_e32 v163, v148
	v_exp_f32_e32 v148, v146
	v_mul_f32_e32 v147, 0xbfb8aa3b, v147
	v_exp_f32_e32 v162, v150
	v_lshlrev_b32_e32 v146, 16, v151
	v_and_b32_e32 v150, 0xffff0000, v151
	v_exp_f32_e32 v151, v147
	v_mul_f32_e32 v146, 0xbfb8aa3b, v146
	v_add_f32_e32 v148, 1.0, v148
	v_mul_f32_e32 v147, 0xbfb8aa3b, v150
	v_exp_f32_e32 v146, v146
	v_exp_f32_e32 v147, v147
	v_rcp_f32_e32 v150, v148
	v_add_f32_e32 v148, 1.0, v151
	v_rcp_f32_e32 v151, v148
	v_pk_add_f32 v[146:147], v[146:147], 1.0 op_sel_hi:[1,0]
	v_mul_f32_e32 v158, 0xbfb8aa3b, v158
	v_exp_f32_e32 v158, v158
	v_pk_mul_f32 v[146:147], v[146:147], v[150:151]
	v_pk_add_f32 v[150:151], v[162:163], 1.0 op_sel_hi:[1,0]
	v_pk_mul_f32 v[120:121], v[120:121], v[146:147]
	v_lshlrev_b32_e32 v146, 16, v149
	v_mul_f32_e32 v146, 0xbfb8aa3b, v146
	v_exp_f32_e32 v147, v146
	v_and_b32_e32 v149, 0xffff0000, v149
	v_mul_f32_e32 v149, 0xbfb8aa3b, v149
	v_exp_f32_e32 v149, v149
	v_lshlrev_b32_e32 v146, 16, v153
	v_add_f32_e32 v148, 1.0, v147
	v_and_b32_e32 v147, 0xffff0000, v153
	v_mul_f32_e32 v146, 0xbfb8aa3b, v146
	v_mul_f32_e32 v147, 0xbfb8aa3b, v147
	v_exp_f32_e32 v146, v146
	v_exp_f32_e32 v147, v147
	v_add_f32_e32 v149, 1.0, v149
	v_rcp_f32_e32 v148, v148
	v_rcp_f32_e32 v149, v149
	v_pk_add_f32 v[146:147], v[146:147], 1.0 op_sel_hi:[1,0]
	v_pk_mul_f32 v[150:151], v[150:151], v[164:165]
	v_pk_mul_f32 v[166:167], v[166:167], v[168:169]
	v_pk_mul_f32 v[146:147], v[146:147], v[148:149]
	v_pk_mul_f32 v[106:107], v[106:107], v[150:151]
	v_pk_mul_f32 v[108:109], v[108:109], v[146:147]
	v_lshlrev_b32_e32 v146, 16, v138
	v_and_b32_e32 v138, 0xffff0000, v138
	v_mul_f32_e32 v138, 0xbfb8aa3b, v138
	v_exp_f32_e32 v138, v138
	v_mul_f32_e32 v146, 0xbfb8aa3b, v146
	v_exp_f32_e32 v147, v146
	v_lshlrev_b32_e32 v146, 16, v142
	v_add_f32_e32 v138, 1.0, v138
	v_rcp_f32_e32 v149, v138
	v_lshlrev_b32_e32 v138, 16, v140
	v_mul_f32_e32 v138, 0xbfb8aa3b, v138
	v_exp_f32_e32 v138, v138
	v_and_b32_e32 v142, 0xffff0000, v142
	v_add_f32_e32 v147, 1.0, v147
	v_mul_f32_e32 v142, 0xbfb8aa3b, v142
	v_add_f32_e32 v138, 1.0, v138
	v_rcp_f32_e32 v152, v138
	v_and_b32_e32 v138, 0xffff0000, v140
	v_mul_f32_e32 v138, 0xbfb8aa3b, v138
	v_exp_f32_e32 v138, v138
	v_and_b32_e32 v140, 0xffff0000, v144
	v_rcp_f32_e32 v148, v147
	v_exp_f32_e32 v147, v142
	v_add_f32_e32 v138, 1.0, v138
	v_rcp_f32_e32 v153, v138
	v_lshlrev_b32_e32 v138, 16, v139
	v_lshlrev_b32_e32 v142, 16, v144
	v_mul_f32_e32 v140, 0xbfb8aa3b, v140
	v_mul_f32_e32 v138, 0xbfb8aa3b, v138
	v_and_b32_e32 v139, 0xffff0000, v139
	v_mul_f32_e32 v142, 0xbfb8aa3b, v142
	v_exp_f32_e32 v151, v140
	v_exp_f32_e32 v140, v138
	v_mul_f32_e32 v139, 0xbfb8aa3b, v139
	v_exp_f32_e32 v150, v142
	v_lshlrev_b32_e32 v138, 16, v143
	v_and_b32_e32 v142, 0xffff0000, v143
	v_exp_f32_e32 v143, v139
	v_mul_f32_e32 v138, 0xbfb8aa3b, v138
	v_add_f32_e32 v140, 1.0, v140
	v_mul_f32_e32 v139, 0xbfb8aa3b, v142
	v_exp_f32_e32 v138, v138
	v_exp_f32_e32 v139, v139
	v_rcp_f32_e32 v142, v140
	v_add_f32_e32 v140, 1.0, v143
	v_rcp_f32_e32 v143, v140
	v_pk_add_f32 v[138:139], v[138:139], 1.0 op_sel_hi:[1,0]
	v_mul_f32_e32 v146, 0xbfb8aa3b, v146
	v_exp_f32_e32 v146, v146
	v_pk_mul_f32 v[138:139], v[138:139], v[142:143]
	v_pk_add_f32 v[142:143], v[150:151], 1.0 op_sel_hi:[1,0]
	v_pk_mul_f32 v[96:97], v[96:97], v[138:139]
	v_lshlrev_b32_e32 v138, 16, v141
	v_mul_f32_e32 v138, 0xbfb8aa3b, v138
	v_exp_f32_e32 v139, v138
	v_and_b32_e32 v141, 0xffff0000, v141
	v_mul_f32_e32 v141, 0xbfb8aa3b, v141
	v_exp_f32_e32 v141, v141
	v_lshlrev_b32_e32 v138, 16, v145
	v_add_f32_e32 v140, 1.0, v139
	v_and_b32_e32 v139, 0xffff0000, v145
	v_mul_f32_e32 v138, 0xbfb8aa3b, v138
	v_mul_f32_e32 v139, 0xbfb8aa3b, v139
	v_exp_f32_e32 v138, v138
	v_exp_f32_e32 v139, v139
	v_add_f32_e32 v141, 1.0, v141
	v_rcp_f32_e32 v140, v140
	v_rcp_f32_e32 v141, v141
	v_pk_add_f32 v[138:139], v[138:139], 1.0 op_sel_hi:[1,0]
	v_pk_mul_f32 v[142:143], v[142:143], v[152:153]
	v_pk_add_f32 v[158:159], v[158:159], 1.0 op_sel_hi:[1,0]
	v_pk_mul_f32 v[138:139], v[138:139], v[140:141]
	v_pk_mul_f32 v[82:83], v[82:83], v[142:143]
	v_pk_mul_f32 v[84:85], v[84:85], v[138:139]
	v_lshlrev_b32_e32 v138, 16, v130
	v_and_b32_e32 v130, 0xffff0000, v130
	v_mul_f32_e32 v130, 0xbfb8aa3b, v130
	v_exp_f32_e32 v130, v130
	v_mul_f32_e32 v138, 0xbfb8aa3b, v138
	v_exp_f32_e32 v139, v138
	v_lshlrev_b32_e32 v138, 16, v134
	v_add_f32_e32 v130, 1.0, v130
	v_rcp_f32_e32 v141, v130
	v_lshlrev_b32_e32 v130, 16, v132
	v_mul_f32_e32 v130, 0xbfb8aa3b, v130
	v_exp_f32_e32 v130, v130
	v_and_b32_e32 v134, 0xffff0000, v134
	v_add_f32_e32 v139, 1.0, v139
	v_mul_f32_e32 v134, 0xbfb8aa3b, v134
	v_add_f32_e32 v130, 1.0, v130
	v_rcp_f32_e32 v144, v130
	v_and_b32_e32 v130, 0xffff0000, v132
	v_mul_f32_e32 v130, 0xbfb8aa3b, v130
	v_exp_f32_e32 v130, v130
	v_and_b32_e32 v132, 0xffff0000, v136
	v_rcp_f32_e32 v140, v139
	v_exp_f32_e32 v139, v134
	v_add_f32_e32 v130, 1.0, v130
	v_rcp_f32_e32 v145, v130
	v_lshlrev_b32_e32 v130, 16, v131
	v_lshlrev_b32_e32 v134, 16, v136
	v_mul_f32_e32 v132, 0xbfb8aa3b, v132
	v_mul_f32_e32 v130, 0xbfb8aa3b, v130
	v_and_b32_e32 v131, 0xffff0000, v131
	v_mul_f32_e32 v134, 0xbfb8aa3b, v134
	v_exp_f32_e32 v143, v132
	v_exp_f32_e32 v132, v130
	v_mul_f32_e32 v131, 0xbfb8aa3b, v131
	v_exp_f32_e32 v142, v134
	v_lshlrev_b32_e32 v130, 16, v135
	v_and_b32_e32 v134, 0xffff0000, v135
	v_exp_f32_e32 v135, v131
	v_mul_f32_e32 v130, 0xbfb8aa3b, v130
	v_add_f32_e32 v132, 1.0, v132
	v_mul_f32_e32 v131, 0xbfb8aa3b, v134
	v_exp_f32_e32 v130, v130
	v_exp_f32_e32 v131, v131
	v_rcp_f32_e32 v134, v132
	v_add_f32_e32 v132, 1.0, v135
	v_rcp_f32_e32 v135, v132
	v_pk_add_f32 v[130:131], v[130:131], 1.0 op_sel_hi:[1,0]
	v_mul_f32_e32 v138, 0xbfb8aa3b, v138
	v_exp_f32_e32 v138, v138
	v_pk_mul_f32 v[130:131], v[130:131], v[134:135]
	v_pk_mul_f32 v[122:123], v[122:123], v[166:167]
	v_pk_mul_f32 v[68:69], v[68:69], v[130:131]
	v_lshlrev_b32_e32 v130, 16, v133
	v_mul_f32_e32 v130, 0xbfb8aa3b, v130
	v_exp_f32_e32 v131, v130
	v_and_b32_e32 v133, 0xffff0000, v133
	v_mul_f32_e32 v133, 0xbfb8aa3b, v133
	v_exp_f32_e32 v133, v133
	v_lshlrev_b32_e32 v130, 16, v137
	v_add_f32_e32 v132, 1.0, v131
	v_and_b32_e32 v131, 0xffff0000, v137
	v_mul_f32_e32 v130, 0xbfb8aa3b, v130
	v_mul_f32_e32 v131, 0xbfb8aa3b, v131
	v_exp_f32_e32 v130, v130
	v_exp_f32_e32 v131, v131
	v_add_f32_e32 v133, 1.0, v133
	v_rcp_f32_e32 v132, v132
	v_rcp_f32_e32 v133, v133
	v_pk_mul_f32 v[158:159], v[158:159], v[160:161]
	v_pk_add_f32 v[146:147], v[146:147], 1.0 op_sel_hi:[1,0]
	v_pk_mul_f32 v[118:119], v[118:119], v[158:159]
	v_pk_mul_f32 v[146:147], v[146:147], v[148:149]
	v_pk_add_f32 v[138:139], v[138:139], 1.0 op_sel_hi:[1,0]
	v_pk_add_f32 v[130:131], v[130:131], 1.0 op_sel_hi:[1,0]
	v_pk_add_f32 v[134:135], v[142:143], 1.0 op_sel_hi:[1,0]
	v_pk_mul_f32 v[94:95], v[94:95], v[146:147]
	v_pk_mul_f32 v[138:139], v[138:139], v[140:141]
	v_pk_mul_f32 v[134:135], v[134:135], v[144:145]
	v_pk_mul_f32 v[130:131], v[130:131], v[132:133]
	v_pk_mul_f32 v[66:67], v[66:67], v[138:139]
	v_pk_mul_f32 v[60:61], v[60:61], v[130:131]
	v_pk_mul_f32 v[58:59], v[58:59], v[134:135]
	s_nop 0
	s_nop 0
	s_waitcnt vmcnt(0)
	s_nop 0
	v_lshlrev_b32_e32 v157, 16, v174
	v_mul_f32_e32 v157, 0xbfb8aa3b, v157
	v_exp_f32_e32 v157, v157
	v_lshlrev_b32_e32 v166, 16, v178
	v_mul_f32_e32 v166, 0xbfb8aa3b, v166
	v_exp_f32_e32 v166, v166
	v_add_f32_e32 v157, 1.0, v157
	v_rcp_f32_e32 v168, v157
	v_and_b32_e32 v157, 0xffff0000, v174
	v_mul_f32_e32 v157, 0xbfb8aa3b, v157
	v_exp_f32_e32 v157, v157
	v_and_b32_e32 v174, 0xffff0000, v178
	v_mul_f32_e32 v174, 0xbfb8aa3b, v174
	v_exp_f32_e32 v167, v174
	v_add_f32_e32 v157, 1.0, v157
	v_rcp_f32_e32 v169, v157
	v_lshlrev_b32_e32 v157, 16, v176
	v_mul_f32_e32 v157, 0xbfb8aa3b, v157
	v_exp_f32_e32 v157, v157
	v_lshlrev_b32_e32 v174, 16, v180
	v_mul_f32_e32 v174, 0xbfb8aa3b, v174
	v_exp_f32_e32 v170, v174
	v_add_f32_e32 v157, 1.0, v157
	v_rcp_f32_e32 v172, v157
	v_and_b32_e32 v157, 0xffff0000, v176
	v_mul_f32_e32 v157, 0xbfb8aa3b, v157
	v_exp_f32_e32 v157, v157
	v_and_b32_e32 v174, 0xffff0000, v180
	v_mul_f32_e32 v174, 0xbfb8aa3b, v174
	v_exp_f32_e32 v171, v174
	v_add_f32_e32 v157, 1.0, v157
	v_rcp_f32_e32 v173, v157
	v_lshlrev_b32_e32 v157, 16, v175
	v_mul_f32_e32 v157, 0xbfb8aa3b, v157
	v_and_b32_e32 v175, 0xffff0000, v175
	v_exp_f32_e32 v157, v157
	v_mul_f32_e32 v175, 0xbfb8aa3b, v175
	v_lshlrev_b32_e32 v174, 16, v179
	v_and_b32_e32 v176, 0xffff0000, v179
	v_exp_f32_e32 v179, v175
	v_add_f32_e32 v157, 1.0, v157
	v_rcp_f32_e32 v178, v157
	v_mul_f32_e32 v174, 0xbfb8aa3b, v174
	v_add_f32_e32 v157, 1.0, v179
	v_rcp_f32_e32 v179, v157
	v_lshlrev_b32_e32 v157, 16, v177
	v_mul_f32_e32 v175, 0xbfb8aa3b, v176
	v_mul_f32_e32 v157, 0xbfb8aa3b, v157
	v_and_b32_e32 v176, 0xffff0000, v177
	v_exp_f32_e32 v174, v174
	v_exp_f32_e32 v175, v175
	v_exp_f32_e32 v157, v157
	v_mul_f32_e32 v176, 0xbfb8aa3b, v176
	v_exp_f32_e32 v177, v176
	v_pk_add_f32 v[174:175], v[174:175], 1.0 op_sel_hi:[1,0]
	v_add_f32_e32 v157, 1.0, v157
	v_pk_mul_f32 v[174:175], v[174:175], v[178:179]
	v_rcp_f32_e32 v176, v157
	v_add_f32_e32 v157, 1.0, v177
	v_pk_mul_f32 v[40:41], v[40:41], v[174:175]
	v_lshlrev_b32_e32 v174, 16, v181
	v_and_b32_e32 v175, 0xffff0000, v181
	v_rcp_f32_e32 v177, v157
	v_lshlrev_b32_e32 v157, 16, v182
	v_and_b32_e32 v182, 0xffff0000, v182
	v_mul_f32_e32 v174, 0xbfb8aa3b, v174
	v_mul_f32_e32 v175, 0xbfb8aa3b, v175
	v_mul_f32_e32 v182, 0xbfb8aa3b, v182
	v_exp_f32_e32 v174, v174
	v_exp_f32_e32 v175, v175
	v_exp_f32_e32 v182, v182
	v_pk_add_f32 v[178:179], v[170:171], 1.0 op_sel_hi:[1,0]
	v_mul_f32_e32 v157, 0xbfb8aa3b, v157
	v_pk_add_f32 v[174:175], v[174:175], 1.0 op_sel_hi:[1,0]
	v_add_f32_e32 v182, 1.0, v182
	v_pk_mul_f32 v[174:175], v[174:175], v[176:177]
	v_rcp_f32_e32 v177, v182
	v_lshlrev_b32_e32 v182, 16, v184
	v_mul_f32_e32 v182, 0xbfb8aa3b, v182
	v_exp_f32_e32 v182, v182
	v_pk_mul_f32 v[28:29], v[28:29], v[174:175]
	v_lshlrev_b32_e32 v174, 16, v208
	v_and_b32_e32 v208, 0xffff0000, v208
	v_add_f32_e32 v182, 1.0, v182
	v_rcp_f32_e32 v180, v182
	v_and_b32_e32 v182, 0xffff0000, v184
	v_mul_f32_e32 v182, 0xbfb8aa3b, v182
	v_exp_f32_e32 v182, v182
	v_mul_f32_e32 v208, 0xbfb8aa3b, v208
	v_and_b32_e32 v184, 0xffff0000, v210
	v_pk_mul_f32 v[178:179], v[178:179], v[172:173]
	v_add_f32_e32 v182, 1.0, v182
	v_rcp_f32_e32 v181, v182
	v_lshlrev_b32_e32 v182, 16, v183
	v_exp_f32_e32 v175, v208
	v_lshlrev_b32_e32 v208, 16, v210
	v_mul_f32_e32 v184, 0xbfb8aa3b, v184
	v_mul_f32_e32 v182, 0xbfb8aa3b, v182
	v_and_b32_e32 v183, 0xffff0000, v183
	v_pk_mul_f32 v[26:27], v[26:27], v[178:179]
	v_mul_f32_e32 v208, 0xbfb8aa3b, v208
	v_exp_f32_e32 v179, v184
	v_exp_f32_e32 v184, v182
	v_mul_f32_e32 v183, 0xbfb8aa3b, v183
	v_exp_f32_e32 v178, v208
	v_lshlrev_b32_e32 v182, 16, v209
	v_and_b32_e32 v208, 0xffff0000, v209
	v_exp_f32_e32 v209, v183
	v_mul_f32_e32 v182, 0xbfb8aa3b, v182
	v_add_f32_e32 v184, 1.0, v184
	v_mul_f32_e32 v183, 0xbfb8aa3b, v208
	v_exp_f32_e32 v182, v182
	v_exp_f32_e32 v183, v183
	v_rcp_f32_e32 v208, v184
	v_add_f32_e32 v184, 1.0, v209
	v_rcp_f32_e32 v209, v184
	v_pk_add_f32 v[182:183], v[182:183], 1.0 op_sel_hi:[1,0]
	v_exp_f32_e32 v157, v157
	v_mul_f32_e32 v174, 0xbfb8aa3b, v174
	v_pk_mul_f32 v[182:183], v[182:183], v[208:209]
	v_pk_add_f32 v[208:209], v[178:179], 1.0 op_sel_hi:[1,0]
	v_pk_mul_f32 v[24:25], v[24:25], v[182:183]
	v_lshlrev_b32_e32 v182, 16, v185
	v_mul_f32_e32 v182, 0xbfb8aa3b, v182
	v_exp_f32_e32 v183, v182
	v_and_b32_e32 v185, 0xffff0000, v185
	v_mul_f32_e32 v185, 0xbfb8aa3b, v185
	v_exp_f32_e32 v185, v185
	v_lshlrev_b32_e32 v182, 16, v211
	v_add_f32_e32 v184, 1.0, v183
	v_and_b32_e32 v183, 0xffff0000, v211
	v_mul_f32_e32 v182, 0xbfb8aa3b, v182
	v_mul_f32_e32 v183, 0xbfb8aa3b, v183
	v_exp_f32_e32 v182, v182
	v_exp_f32_e32 v183, v183
	v_add_f32_e32 v185, 1.0, v185
	v_rcp_f32_e32 v184, v184
	v_rcp_f32_e32 v185, v185
	v_pk_add_f32 v[182:183], v[182:183], 1.0 op_sel_hi:[1,0]
	v_pk_mul_f32 v[208:209], v[208:209], v[180:181]
	v_exp_f32_e32 v174, v174
	v_pk_mul_f32 v[182:183], v[182:183], v[184:185]
	v_pk_mul_f32 v[18:19], v[18:19], v[208:209]
	v_pk_mul_f32 v[20:21], v[20:21], v[182:183]
	v_lshlrev_b32_e32 v182, 16, v212
	v_and_b32_e32 v212, 0xffff0000, v212
	v_mul_f32_e32 v212, 0xbfb8aa3b, v212
	v_exp_f32_e32 v212, v212
	v_mul_f32_e32 v182, 0xbfb8aa3b, v182
	v_exp_f32_e32 v183, v182
	v_lshlrev_b32_e32 v182, 16, v216
	v_add_f32_e32 v212, 1.0, v212
	v_rcp_f32_e32 v185, v212
	v_lshlrev_b32_e32 v212, 16, v214
	v_mul_f32_e32 v212, 0xbfb8aa3b, v212
	v_exp_f32_e32 v212, v212
	v_and_b32_e32 v216, 0xffff0000, v216
	v_add_f32_e32 v183, 1.0, v183
	v_mul_f32_e32 v216, 0xbfb8aa3b, v216
	v_add_f32_e32 v212, 1.0, v212
	v_rcp_f32_e32 v210, v212
	v_and_b32_e32 v212, 0xffff0000, v214
	v_mul_f32_e32 v212, 0xbfb8aa3b, v212
	v_exp_f32_e32 v212, v212
	v_and_b32_e32 v214, 0xffff0000, v218
	v_rcp_f32_e32 v184, v183
	v_exp_f32_e32 v183, v216
	v_add_f32_e32 v212, 1.0, v212
	v_rcp_f32_e32 v211, v212
	v_lshlrev_b32_e32 v212, 16, v213
	v_lshlrev_b32_e32 v216, 16, v218
	v_mul_f32_e32 v214, 0xbfb8aa3b, v214
	v_mul_f32_e32 v212, 0xbfb8aa3b, v212
	v_and_b32_e32 v213, 0xffff0000, v213
	v_mul_f32_e32 v216, 0xbfb8aa3b, v216
	v_exp_f32_e32 v209, v214
	v_exp_f32_e32 v214, v212
	v_mul_f32_e32 v213, 0xbfb8aa3b, v213
	v_exp_f32_e32 v208, v216
	v_lshlrev_b32_e32 v212, 16, v217
	v_and_b32_e32 v216, 0xffff0000, v217
	v_exp_f32_e32 v217, v213
	v_mul_f32_e32 v212, 0xbfb8aa3b, v212
	v_add_f32_e32 v214, 1.0, v214
	v_mul_f32_e32 v213, 0xbfb8aa3b, v216
	v_exp_f32_e32 v212, v212
	v_exp_f32_e32 v213, v213
	v_rcp_f32_e32 v216, v214
	v_add_f32_e32 v214, 1.0, v217
	v_rcp_f32_e32 v217, v214
	v_pk_add_f32 v[212:213], v[212:213], 1.0 op_sel_hi:[1,0]
	v_add_f32_e32 v157, 1.0, v157
	v_mul_f32_e32 v182, 0xbfb8aa3b, v182
	v_pk_mul_f32 v[212:213], v[212:213], v[216:217]
	v_pk_add_f32 v[216:217], v[208:209], 1.0 op_sel_hi:[1,0]
	v_pk_mul_f32 v[16:17], v[16:17], v[212:213]
	v_lshlrev_b32_e32 v212, 16, v215
	v_mul_f32_e32 v212, 0xbfb8aa3b, v212
	v_exp_f32_e32 v213, v212
	v_and_b32_e32 v215, 0xffff0000, v215
	v_mul_f32_e32 v215, 0xbfb8aa3b, v215
	v_exp_f32_e32 v215, v215
	v_lshlrev_b32_e32 v212, 16, v219
	v_add_f32_e32 v214, 1.0, v213
	v_and_b32_e32 v213, 0xffff0000, v219
	v_mul_f32_e32 v212, 0xbfb8aa3b, v212
	v_mul_f32_e32 v213, 0xbfb8aa3b, v213
	v_exp_f32_e32 v212, v212
	v_exp_f32_e32 v213, v213
	v_add_f32_e32 v215, 1.0, v215
	v_rcp_f32_e32 v214, v214
	v_rcp_f32_e32 v215, v215
	v_pk_add_f32 v[212:213], v[212:213], 1.0 op_sel_hi:[1,0]
	v_pk_mul_f32 v[216:217], v[216:217], v[210:211]
	v_rcp_f32_e32 v176, v157
	v_pk_mul_f32 v[212:213], v[212:213], v[214:215]
	v_pk_mul_f32 v[10:11], v[10:11], v[216:217]
	v_pk_mul_f32 v[12:13], v[12:13], v[212:213]
	v_lshlrev_b32_e32 v212, 16, v220
	v_and_b32_e32 v220, 0xffff0000, v220
	v_mul_f32_e32 v220, 0xbfb8aa3b, v220
	v_exp_f32_e32 v220, v220
	v_mul_f32_e32 v212, 0xbfb8aa3b, v212
	v_exp_f32_e32 v213, v212
	v_lshlrev_b32_e32 v212, 16, v230
	v_add_f32_e32 v220, 1.0, v220
	v_rcp_f32_e32 v215, v220
	v_lshlrev_b32_e32 v220, 16, v222
	v_mul_f32_e32 v220, 0xbfb8aa3b, v220
	v_exp_f32_e32 v220, v220
	v_and_b32_e32 v230, 0xffff0000, v230
	v_add_f32_e32 v213, 1.0, v213
	v_mul_f32_e32 v230, 0xbfb8aa3b, v230
	v_add_f32_e32 v220, 1.0, v220
	v_rcp_f32_e32 v218, v220
	v_and_b32_e32 v220, 0xffff0000, v222
	v_mul_f32_e32 v220, 0xbfb8aa3b, v220
	v_exp_f32_e32 v220, v220
	v_and_b32_e32 v222, 0xffff0000, v232
	v_rcp_f32_e32 v214, v213
	v_exp_f32_e32 v213, v230
	v_add_f32_e32 v220, 1.0, v220
	v_rcp_f32_e32 v219, v220
	v_lshlrev_b32_e32 v220, 16, v221
	v_lshlrev_b32_e32 v230, 16, v232
	v_mul_f32_e32 v222, 0xbfb8aa3b, v222
	v_mul_f32_e32 v220, 0xbfb8aa3b, v220
	v_and_b32_e32 v221, 0xffff0000, v221
	v_mul_f32_e32 v230, 0xbfb8aa3b, v230
	v_exp_f32_e32 v217, v222
	v_exp_f32_e32 v222, v220
	v_mul_f32_e32 v221, 0xbfb8aa3b, v221
	v_exp_f32_e32 v216, v230
	v_lshlrev_b32_e32 v220, 16, v231
	v_and_b32_e32 v230, 0xffff0000, v231
	v_exp_f32_e32 v231, v221
	v_mul_f32_e32 v220, 0xbfb8aa3b, v220
	v_add_f32_e32 v222, 1.0, v222
	v_mul_f32_e32 v221, 0xbfb8aa3b, v230
	v_exp_f32_e32 v220, v220
	v_exp_f32_e32 v221, v221
	v_rcp_f32_e32 v230, v222
	v_add_f32_e32 v222, 1.0, v231
	v_rcp_f32_e32 v231, v222
	v_pk_add_f32 v[220:221], v[220:221], 1.0 op_sel_hi:[1,0]
	v_exp_f32_e32 v182, v182
	v_mul_f32_e32 v212, 0xbfb8aa3b, v212
	v_pk_mul_f32 v[220:221], v[220:221], v[230:231]
	v_exp_f32_e32 v212, v212
	v_pk_mul_f32 v[8:9], v[8:9], v[220:221]
	v_lshlrev_b32_e32 v220, 16, v223
	v_mul_f32_e32 v220, 0xbfb8aa3b, v220
	v_exp_f32_e32 v221, v220
	v_and_b32_e32 v223, 0xffff0000, v223
	v_mul_f32_e32 v223, 0xbfb8aa3b, v223
	v_exp_f32_e32 v223, v223
	v_lshlrev_b32_e32 v220, 16, v233
	v_add_f32_e32 v222, 1.0, v221
	v_and_b32_e32 v221, 0xffff0000, v233
	v_mul_f32_e32 v220, 0xbfb8aa3b, v220
	v_mul_f32_e32 v221, 0xbfb8aa3b, v221
	v_exp_f32_e32 v220, v220
	v_exp_f32_e32 v221, v221
	v_add_f32_e32 v223, 1.0, v223
	v_pk_add_f32 v[166:167], v[166:167], 1.0 op_sel_hi:[1,0]
	v_rcp_f32_e32 v222, v222
	v_rcp_f32_e32 v223, v223
	v_pk_mul_f32 v[166:167], v[166:167], v[168:169]
	v_pk_add_f32 v[174:175], v[174:175], 1.0 op_sel_hi:[1,0]
	v_pk_mul_f32 v[38:39], v[38:39], v[166:167]
	v_pk_mul_f32 v[174:175], v[174:175], v[176:177]
	v_pk_add_f32 v[182:183], v[182:183], 1.0 op_sel_hi:[1,0]
	v_pk_mul_f32 v[22:23], v[22:23], v[174:175]
	v_pk_mul_f32 v[182:183], v[182:183], v[184:185]
	v_pk_add_f32 v[212:213], v[212:213], 1.0 op_sel_hi:[1,0]
	v_pk_add_f32 v[220:221], v[220:221], 1.0 op_sel_hi:[1,0]
	v_pk_add_f32 v[230:231], v[216:217], 1.0 op_sel_hi:[1,0]
	v_pk_mul_f32 v[14:15], v[14:15], v[182:183]
	v_pk_mul_f32 v[212:213], v[212:213], v[214:215]
	v_pk_mul_f32 v[230:231], v[230:231], v[218:219]
	v_pk_mul_f32 v[220:221], v[220:221], v[222:223]
	v_pk_mul_f32 v[6:7], v[6:7], v[212:213]
	v_pk_mul_f32 v[4:5], v[4:5], v[220:221]
	v_pk_mul_f32 v[2:3], v[2:3], v[230:231]
	s_nop 0
	s_add_u32 s64, s64, 0xc0880
	s_addc_u32 s65, s65, 0
	s_add_u32 s35, s62, 0x900
	s_addc_u32 s74, s63, 0
	s_mov_b32 s90, 14
